# plus: PLE-up epilogue reads of h and gate G (single-use streams) use nt loads
# speedup vs baseline: 1.0089x; 1.0089x over previous
; __device__ __forceinline__ unsigned cvt_pk_bf16(float lo, float hi) { return pk2(lo, hi); }
;     __device__ __forceinline__ void operator()(const f32x4 (&acc)[2][2][4][2], const Unit& u, int wr, int wc, int fr, int fq) const {
;     ...
;                 for (int bj = 0; bj < 2; ++bj) { const u32x4 x = hv[m][bj], g = gv[m][bj]; const f32x4 a0 = acc[ai][bj][m][0], a1 = acc[ai][bj][m][1];
;                     u32x4 w; w.x = cvt_pk_bf16(bflo(x.x) + a0[0] * bflo(g.x), bfhi(x.x) + a0[1] * bfhi(g.x)); w.y = cvt_pk_bf16(bflo(x.y) + a0[2] * bflo(g.y), bfhi(x.y) + a0[3] * bfhi(g.y));
;                     w.z = cvt_pk_bf16(bflo(x.z) + a1[0] * bflo(g.z), bfhi(x.z) + a1[1] * bfhi(g.z)); w.w = cvt_pk_bf16(bflo(x.w) + a1[2] * bflo(g.w), bfhi(x.w) + a1[3] * bfhi(g.w));
;                     *(u32x4*)(hn + ro0 + (size_t)m * 16 * DM + bj * HALF) = w; }
;             asm volatile("" ::: "memory");
.LBB0_1210:
	v_lshl_add_u32 v130, s20, 8, v1
	v_lshl_or_b32 v132, s21, 8, v222
	v_ashrrev_i32_e32 v131, 31, v130
	v_ashrrev_i32_e32 v133, 31, v132
	v_lshlrev_b64 v[130:131], 10, v[130:131]
	v_lshl_add_u64 v[130:131], v[130:131], 0, v[132:133]
	v_lshlrev_b64 v[204:205], 1, v[130:131]
	v_lshl_add_u64 v[130:131], s[8:9], 0, v[204:205]
	v_lshl_add_u64 v[132:133], s[10:11], 0, v[204:205]
	global_load_dwordx4 v[224:227], v[130:131], off nt
	global_load_dwordx4 v[228:231], v[132:133], off nt
	global_load_dwordx4 v[182:185], v[130:131], off offset:256 nt
	global_load_dwordx4 v[178:181], v[132:133], off offset:256 nt
	v_add_co_u32_e32 v134, vcc, s86, v130
	s_mov_b64 s[20:21], 0x40000
	s_nop 0
	v_addc_co_u32_e32 v135, vcc, 0, v131, vcc
	global_load_dwordx4 v[170:173], v[134:135], off nt
	v_add_co_u32_e32 v136, vcc, s86, v132
	s_movk_i32 s56, 0x104
	s_nop 0
	v_addc_co_u32_e32 v137, vcc, 0, v133, vcc
	global_load_dwordx4 v[174:177], v[136:137], off nt
	global_load_dwordx4 v[166:169], v[134:135], off offset:256 nt
	global_load_dwordx4 v[162:165], v[136:137], off offset:256 nt
	v_add_co_u32_e32 v134, vcc, s84, v130
	s_mov_b64 s[36:37], 0x2000
	s_nop 0
	v_addc_co_u32_e32 v135, vcc, 0, v131, vcc
	global_load_dwordx4 v[158:161], v[134:135], off nt
	v_add_co_u32_e32 v136, vcc, s84, v132
	s_mov_b32 s62, 0x3b000000
	s_nop 0
	v_addc_co_u32_e32 v137, vcc, 0, v133, vcc
	global_load_dwordx4 v[154:157], v[136:137], off nt
	global_load_dwordx4 v[150:153], v[134:135], off offset:256 nt
	global_load_dwordx4 v[146:149], v[136:137], off offset:256 nt
	v_add_co_u32_e32 v130, vcc, s85, v130
	s_mov_b32 s58, 0x358637bd
	s_nop 0
	v_addc_co_u32_e32 v131, vcc, 0, v131, vcc
	global_load_dwordx4 v[142:145], v[130:131], off nt
	v_add_co_u32_e32 v132, vcc, s85, v132
	s_waitcnt vmcnt(0)
	v_lshlrev_b32_e32 v218, 16, v224
	v_addc_co_u32_e32 v133, vcc, 0, v133, vcc
	global_load_dwordx4 v[138:141], v[132:133], off nt
	global_load_dwordx4 v[134:137], v[130:131], off offset:256 nt
	s_nop 0
	global_load_dwordx4 v[130:133], v[132:133], off offset:256 nt
	v_and_b32_e32 v219, 0xffff0000, v224
	v_lshlrev_b32_e32 v232, 16, v228
	v_and_b32_e32 v233, 0xffff0000, v228
	v_pk_fma_f32 v[126:127], v[126:127], v[232:233], v[218:219]
	v_lshlrev_b32_e32 v218, 16, v225
	v_and_b32_e32 v219, 0xffff0000, v225
	v_lshlrev_b32_e32 v224, 16, v229
	v_and_b32_e32 v225, 0xffff0000, v229
	v_pk_fma_f32 v[128:129], v[128:129], v[224:225], v[218:219]
	v_cvt_pk_bf16_f32 v126, v126, v127
	v_cvt_pk_bf16_f32 v127, v128, v129
	v_lshlrev_b32_e32 v128, 16, v226
	v_and_b32_e32 v129, 0xffff0000, v226
	v_lshlrev_b32_e32 v218, 16, v230
	v_and_b32_e32 v219, 0xffff0000, v230
	v_pk_fma_f32 v[122:123], v[122:123], v[218:219], v[128:129]
	v_lshlrev_b32_e32 v218, 16, v231
	v_cvt_pk_bf16_f32 v128, v122, v123
	v_lshlrev_b32_e32 v122, 16, v227
	v_and_b32_e32 v123, 0xffff0000, v227
	v_and_b32_e32 v219, 0xffff0000, v231
	v_pk_fma_f32 v[122:123], v[124:125], v[218:219], v[122:123]
	v_lshlrev_b32_e32 v124, 16, v182
	v_cvt_pk_bf16_f32 v129, v122, v123
	v_lshl_add_u64 v[122:123], s[0:1], 0, v[204:205]
	global_store_dwordx4 v[122:123], v[126:129], off
	v_and_b32_e32 v125, 0xffff0000, v182
	s_nop 0
	v_lshlrev_b32_e32 v126, 16, v178
	v_and_b32_e32 v127, 0xffff0000, v178
	v_pk_fma_f32 v[118:119], v[118:119], v[126:127], v[124:125]
	v_lshlrev_b32_e32 v124, 16, v183
	v_and_b32_e32 v125, 0xffff0000, v183
	v_lshlrev_b32_e32 v126, 16, v179
	v_and_b32_e32 v127, 0xffff0000, v179
	v_pk_fma_f32 v[120:121], v[120:121], v[126:127], v[124:125]
	v_cvt_pk_bf16_f32 v118, v118, v119
	v_cvt_pk_bf16_f32 v119, v120, v121
	v_lshlrev_b32_e32 v120, 16, v184
	v_and_b32_e32 v121, 0xffff0000, v184
	v_lshlrev_b32_e32 v124, 16, v180
	v_and_b32_e32 v125, 0xffff0000, v180
	v_pk_fma_f32 v[110:111], v[110:111], v[124:125], v[120:121]
	v_lshlrev_b32_e32 v124, 16, v181
	v_cvt_pk_bf16_f32 v120, v110, v111
	v_lshlrev_b32_e32 v110, 16, v185
	v_and_b32_e32 v111, 0xffff0000, v185
	v_and_b32_e32 v125, 0xffff0000, v181
	v_pk_fma_f32 v[110:111], v[112:113], v[124:125], v[110:111]
	v_lshlrev_b32_e32 v112, 16, v174
	v_cvt_pk_bf16_f32 v121, v110, v111
	v_lshlrev_b32_e32 v110, 16, v170
	v_and_b32_e32 v111, 0xffff0000, v170
	v_and_b32_e32 v113, 0xffff0000, v174
	v_pk_fma_f32 v[110:111], v[114:115], v[112:113], v[110:111]
	v_lshlrev_b32_e32 v112, 16, v171
	v_and_b32_e32 v113, 0xffff0000, v171
	v_lshlrev_b32_e32 v114, 16, v175
	v_and_b32_e32 v115, 0xffff0000, v175
	v_pk_fma_f32 v[112:113], v[116:117], v[114:115], v[112:113]
	v_cvt_pk_bf16_f32 v110, v110, v111
	v_cvt_pk_bf16_f32 v111, v112, v113
	v_lshlrev_b32_e32 v112, 16, v172
	v_and_b32_e32 v113, 0xffff0000, v172
	v_lshlrev_b32_e32 v114, 16, v176
	v_and_b32_e32 v115, 0xffff0000, v176
	v_pk_fma_f32 v[106:107], v[106:107], v[114:115], v[112:113]
	v_lshlrev_b32_e32 v114, 16, v177
	v_cvt_pk_bf16_f32 v112, v106, v107
	v_lshlrev_b32_e32 v106, 16, v173
	v_and_b32_e32 v107, 0xffff0000, v173
	v_and_b32_e32 v115, 0xffff0000, v177
	v_pk_fma_f32 v[106:107], v[108:109], v[114:115], v[106:107]
	v_lshlrev_b32_e32 v108, 16, v166
	v_cvt_pk_bf16_f32 v113, v106, v107
	v_add_co_u32_e32 v106, vcc, s86, v122
	v_and_b32_e32 v109, 0xffff0000, v166
	s_nop 0
	v_addc_co_u32_e32 v107, vcc, 0, v123, vcc
	global_store_dwordx4 v[106:107], v[110:113], off
	global_store_dwordx4 v[122:123], v[118:121], off offset:256
	s_nop 0
	v_lshlrev_b32_e32 v110, 16, v162
	v_and_b32_e32 v111, 0xffff0000, v162
	v_pk_fma_f32 v[102:103], v[102:103], v[110:111], v[108:109]
	v_lshlrev_b32_e32 v108, 16, v167
	v_and_b32_e32 v109, 0xffff0000, v167
	v_lshlrev_b32_e32 v110, 16, v163
	v_and_b32_e32 v111, 0xffff0000, v163
	v_pk_fma_f32 v[104:105], v[104:105], v[110:111], v[108:109]
; __device__ __forceinline__ unsigned cvt_pk_bf16(float lo, float hi) { return pk2(lo, hi); }
;     __device__ __forceinline__ void operator()(const f32x4 (&acc)[2][2][4][2], const Unit& u, int wr, int wc, int fr, int fq) const {
;     ...
;         for (int ai = 0; ai < 2; ++ai) {
;             const size_t ro0 = (size_t)(row0 + ai * HALF) * DM + col0;
;             u32x4 hv[4][2], gv[4][2];
; #pragma unroll
;             for (int m = 0; m < 4; ++m)
; #pragma unroll
;                 for (int bj = 0; bj < 2; ++bj) { hv[m][bj] = *(const u32x4*)(h + ro0 + (size_t)m * 16 * DM + bj * HALF); gv[m][bj] = *(const u32x4*)(Gt + ro0 + (size_t)m * 16 * DM + bj * HALF); }
; #pragma unroll
;             for (int m = 0; m < 4; ++m)
; #pragma unroll
;                 for (int bj = 0; bj < 2; ++bj) { const u32x4 x = hv[m][bj], g = gv[m][bj]; const f32x4 a0 = acc[ai][bj][m][0], a1 = acc[ai][bj][m][1];
;                     u32x4 w; w.x = cvt_pk_bf16(bflo(x.x) + a0[0] * bflo(g.x), bfhi(x.x) + a0[1] * bfhi(g.x)); w.y = cvt_pk_bf16(bflo(x.y) + a0[2] * bflo(g.y), bfhi(x.y) + a0[3] * bfhi(g.y));
;                     w.z = cvt_pk_bf16(bflo(x.z) + a1[0] * bflo(g.z), bfhi(x.z) + a1[1] * bfhi(g.z)); w.w = cvt_pk_bf16(bflo(x.w) + a1[2] * bflo(g.w), bfhi(x.w) + a1[3] * bfhi(g.w));
;                     *(u32x4*)(hn + ro0 + (size_t)m * 16 * DM + bj * HALF) = w; }
;             asm volatile("" ::: "memory");
	v_cvt_pk_bf16_f32 v102, v102, v103
	v_cvt_pk_bf16_f32 v103, v104, v105
	v_lshlrev_b32_e32 v104, 16, v168
	v_and_b32_e32 v105, 0xffff0000, v168
	v_lshlrev_b32_e32 v108, 16, v164
	v_and_b32_e32 v109, 0xffff0000, v164
	v_pk_fma_f32 v[94:95], v[94:95], v[108:109], v[104:105]
	v_lshlrev_b32_e32 v108, 16, v165
	v_cvt_pk_bf16_f32 v104, v94, v95
	v_lshlrev_b32_e32 v94, 16, v169
	v_and_b32_e32 v95, 0xffff0000, v169
	v_and_b32_e32 v109, 0xffff0000, v165
	v_pk_fma_f32 v[94:95], v[96:97], v[108:109], v[94:95]
	v_lshlrev_b32_e32 v96, 16, v154
	v_cvt_pk_bf16_f32 v105, v94, v95
	v_lshlrev_b32_e32 v94, 16, v158
	v_and_b32_e32 v95, 0xffff0000, v158
	v_and_b32_e32 v97, 0xffff0000, v154
	v_pk_fma_f32 v[94:95], v[98:99], v[96:97], v[94:95]
	v_lshlrev_b32_e32 v96, 16, v159
	v_and_b32_e32 v97, 0xffff0000, v159
	v_lshlrev_b32_e32 v98, 16, v155
	v_and_b32_e32 v99, 0xffff0000, v155
	v_pk_fma_f32 v[96:97], v[100:101], v[98:99], v[96:97]
	v_cvt_pk_bf16_f32 v94, v94, v95
	v_cvt_pk_bf16_f32 v95, v96, v97
	v_lshlrev_b32_e32 v96, 16, v160
	v_and_b32_e32 v97, 0xffff0000, v160
	v_lshlrev_b32_e32 v98, 16, v156
	v_and_b32_e32 v99, 0xffff0000, v156
	v_pk_fma_f32 v[90:91], v[90:91], v[98:99], v[96:97]
	v_lshlrev_b32_e32 v98, 16, v157
	v_cvt_pk_bf16_f32 v96, v90, v91
	v_lshlrev_b32_e32 v90, 16, v161
	v_and_b32_e32 v91, 0xffff0000, v161
	v_and_b32_e32 v99, 0xffff0000, v157
	v_pk_fma_f32 v[90:91], v[92:93], v[98:99], v[90:91]
	v_lshlrev_b32_e32 v92, 16, v150
	v_cvt_pk_bf16_f32 v97, v90, v91
	v_add_co_u32_e32 v90, vcc, s84, v122
	v_and_b32_e32 v93, 0xffff0000, v150
	s_nop 0
	v_addc_co_u32_e32 v91, vcc, 0, v123, vcc
	global_store_dwordx4 v[90:91], v[94:97], off
	global_store_dwordx4 v[106:107], v[102:105], off offset:256
	s_nop 0
	v_lshlrev_b32_e32 v94, 16, v146
	v_and_b32_e32 v95, 0xffff0000, v146
	v_pk_fma_f32 v[86:87], v[86:87], v[94:95], v[92:93]
	v_lshlrev_b32_e32 v92, 16, v151
	v_and_b32_e32 v93, 0xffff0000, v151
	v_lshlrev_b32_e32 v94, 16, v147
	v_and_b32_e32 v95, 0xffff0000, v147
	v_pk_fma_f32 v[88:89], v[88:89], v[94:95], v[92:93]
	v_cvt_pk_bf16_f32 v86, v86, v87
	v_cvt_pk_bf16_f32 v87, v88, v89
	v_lshlrev_b32_e32 v88, 16, v152
	v_and_b32_e32 v89, 0xffff0000, v152
	v_lshlrev_b32_e32 v92, 16, v148
	v_and_b32_e32 v93, 0xffff0000, v148
	v_pk_fma_f32 v[78:79], v[78:79], v[92:93], v[88:89]
	v_lshlrev_b32_e32 v92, 16, v149
	v_cvt_pk_bf16_f32 v88, v78, v79
	v_lshlrev_b32_e32 v78, 16, v153
	v_and_b32_e32 v79, 0xffff0000, v153
	v_and_b32_e32 v93, 0xffff0000, v149
	v_pk_fma_f32 v[78:79], v[80:81], v[92:93], v[78:79]
	s_waitcnt vmcnt(7)
	v_lshlrev_b32_e32 v80, 16, v138
	v_cvt_pk_bf16_f32 v89, v78, v79
	v_lshlrev_b32_e32 v78, 16, v142
	v_and_b32_e32 v79, 0xffff0000, v142
	v_and_b32_e32 v81, 0xffff0000, v138
	v_pk_fma_f32 v[78:79], v[82:83], v[80:81], v[78:79]
	v_lshlrev_b32_e32 v80, 16, v143
	v_and_b32_e32 v81, 0xffff0000, v143
	v_lshlrev_b32_e32 v82, 16, v139
	v_and_b32_e32 v83, 0xffff0000, v139
	v_pk_fma_f32 v[80:81], v[84:85], v[82:83], v[80:81]
	v_cvt_pk_bf16_f32 v78, v78, v79
	v_cvt_pk_bf16_f32 v79, v80, v81
	v_lshlrev_b32_e32 v80, 16, v144
	v_and_b32_e32 v81, 0xffff0000, v144
	v_lshlrev_b32_e32 v82, 16, v140
	v_and_b32_e32 v83, 0xffff0000, v140
	v_pk_fma_f32 v[74:75], v[74:75], v[82:83], v[80:81]
	v_lshlrev_b32_e32 v82, 16, v141
	v_cvt_pk_bf16_f32 v80, v74, v75
	v_lshlrev_b32_e32 v74, 16, v145
	v_and_b32_e32 v75, 0xffff0000, v145
	v_and_b32_e32 v83, 0xffff0000, v141
	v_pk_fma_f32 v[74:75], v[76:77], v[82:83], v[74:75]
	s_waitcnt vmcnt(6)
	v_lshlrev_b32_e32 v76, 16, v134
	v_cvt_pk_bf16_f32 v81, v74, v75
	v_add_co_u32_e32 v74, vcc, s85, v122
	v_and_b32_e32 v77, 0xffff0000, v134
	s_nop 0
	v_addc_co_u32_e32 v75, vcc, 0, v123, vcc
	global_store_dwordx4 v[74:75], v[78:81], off
	global_store_dwordx4 v[90:91], v[86:89], off offset:256
	s_waitcnt vmcnt(7)
	v_lshlrev_b32_e32 v78, 16, v130
	v_and_b32_e32 v79, 0xffff0000, v130
	v_pk_fma_f32 v[70:71], v[70:71], v[78:79], v[76:77]
	v_lshlrev_b32_e32 v76, 16, v135
	v_and_b32_e32 v77, 0xffff0000, v135
	v_lshlrev_b32_e32 v78, 16, v131
	v_and_b32_e32 v79, 0xffff0000, v131
	v_pk_fma_f32 v[72:73], v[72:73], v[78:79], v[76:77]
	v_cvt_pk_bf16_f32 v70, v70, v71
	v_cvt_pk_bf16_f32 v71, v72, v73
	v_lshlrev_b32_e32 v72, 16, v136
	v_and_b32_e32 v73, 0xffff0000, v136
	v_lshlrev_b32_e32 v76, 16, v132
	v_and_b32_e32 v77, 0xffff0000, v132
	v_pk_fma_f32 v[66:67], v[66:67], v[76:77], v[72:73]
	v_lshlrev_b32_e32 v76, 16, v133
	v_cvt_pk_bf16_f32 v72, v66, v67
	v_lshlrev_b32_e32 v66, 16, v137
	v_and_b32_e32 v67, 0xffff0000, v137
	v_and_b32_e32 v77, 0xffff0000, v133
	v_pk_fma_f32 v[66:67], v[68:69], v[76:77], v[66:67]
	v_lshl_add_u64 v[130:131], v[204:205], 0, s[20:21]
	v_cvt_pk_bf16_f32 v73, v66, v67
	global_store_dwordx4 v[74:75], v[70:73], off offset:256
	v_lshl_add_u64 v[66:67], s[8:9], 0, v[130:131]
	v_lshl_add_u64 v[68:69], s[10:11], 0, v[130:131]
	global_load_dwordx4 v[98:101], v[66:67], off nt
	global_load_dwordx4 v[102:105], v[68:69], off nt
	global_load_dwordx4 v[106:109], v[66:67], off offset:256 nt
	global_load_dwordx4 v[110:113], v[68:69], off offset:256 nt
	v_add_co_u32_e32 v70, vcc, s86, v66
	s_mov_b64 s[20:21], -1
	s_nop 0
	v_addc_co_u32_e32 v71, vcc, 0, v67, vcc
	global_load_dwordx4 v[114:117], v[70:71], off nt
	v_add_co_u32_e32 v72, vcc, s86, v68
	s_waitcnt vmcnt(4)
	v_lshlrev_b32_e32 v132, 16, v98
	v_addc_co_u32_e32 v73, vcc, 0, v69, vcc
	global_load_dwordx4 v[118:121], v[72:73], off nt
	global_load_dwordx4 v[122:125], v[70:71], off offset:256 nt
	global_load_dwordx4 v[126:129], v[72:73], off offset:256 nt
	v_add_co_u32_e32 v70, vcc, s84, v66
	v_and_b32_e32 v133, 0xffff0000, v98
	s_nop 0
	v_addc_co_u32_e32 v71, vcc, 0, v67, vcc
	global_load_dwordx4 v[90:93], v[70:71], off nt
	v_add_co_u32_e32 v72, vcc, s84, v68
	s_waitcnt vmcnt(7)
; __device__ __forceinline__ unsigned cvt_pk_bf16(float lo, float hi) { return pk2(lo, hi); }
;     __device__ __forceinline__ void operator()(const f32x4 (&acc)[2][2][4][2], const Unit& u, int wr, int wc, int fr, int fq) const {
;     ...
;                 for (int bj = 0; bj < 2; ++bj) { hv[m][bj] = *(const u32x4*)(h + ro0 + (size_t)m * 16 * DM + bj * HALF); gv[m][bj] = *(const u32x4*)(Gt + ro0 + (size_t)m * 16 * DM + bj * HALF); }
; #pragma unroll
;             for (int m = 0; m < 4; ++m)
; #pragma unroll
;                 for (int bj = 0; bj < 2; ++bj) { const u32x4 x = hv[m][bj], g = gv[m][bj]; const f32x4 a0 = acc[ai][bj][m][0], a1 = acc[ai][bj][m][1];
;                     u32x4 w; w.x = cvt_pk_bf16(bflo(x.x) + a0[0] * bflo(g.x), bfhi(x.x) + a0[1] * bfhi(g.x)); w.y = cvt_pk_bf16(bflo(x.y) + a0[2] * bflo(g.y), bfhi(x.y) + a0[3] * bfhi(g.y));
;                     w.z = cvt_pk_bf16(bflo(x.z) + a1[0] * bflo(g.z), bfhi(x.z) + a1[1] * bfhi(g.z)); w.w = cvt_pk_bf16(bflo(x.w) + a1[2] * bflo(g.w), bfhi(x.w) + a1[3] * bfhi(g.w));
;                     *(u32x4*)(hn + ro0 + (size_t)m * 16 * DM + bj * HALF) = w; }
;             asm volatile("" ::: "memory");
	v_lshlrev_b32_e32 v134, 16, v102
	v_addc_co_u32_e32 v73, vcc, 0, v69, vcc
	global_load_dwordx4 v[94:97], v[72:73], off nt
	global_load_dwordx4 v[82:85], v[70:71], off offset:256 nt
	global_load_dwordx4 v[86:89], v[72:73], off offset:256 nt
	v_add_co_u32_e32 v66, vcc, s85, v66
	v_and_b32_e32 v135, 0xffff0000, v102
	s_nop 0
	v_addc_co_u32_e32 v67, vcc, 0, v67, vcc
	global_load_dwordx4 v[74:77], v[66:67], off nt
	v_add_co_u32_e32 v70, vcc, s85, v68
	v_lshlrev_b32_e32 v98, 16, v99
	s_nop 0
	v_addc_co_u32_e32 v71, vcc, 0, v69, vcc
	global_load_dwordx4 v[78:81], v[70:71], off nt
	s_nop 0
	global_load_dwordx4 v[66:69], v[66:67], off offset:256 nt
	s_nop 0
	global_load_dwordx4 v[70:73], v[70:71], off offset:256 nt
	v_and_b32_e32 v99, 0xffff0000, v99
	v_lshlrev_b32_e32 v102, 16, v103
	v_and_b32_e32 v103, 0xffff0000, v103
	v_pk_fma_f32 v[62:63], v[62:63], v[134:135], v[132:133]
	v_pk_fma_f32 v[64:65], v[64:65], v[102:103], v[98:99]
	v_cvt_pk_bf16_f32 v62, v62, v63
	v_cvt_pk_bf16_f32 v63, v64, v65
	v_lshlrev_b32_e32 v64, 16, v100
	v_and_b32_e32 v65, 0xffff0000, v100
	v_lshlrev_b32_e32 v98, 16, v104
	v_and_b32_e32 v99, 0xffff0000, v104
	v_pk_fma_f32 v[58:59], v[58:59], v[98:99], v[64:65]
	v_lshlrev_b32_e32 v98, 16, v105
	v_cvt_pk_bf16_f32 v64, v58, v59
	v_lshlrev_b32_e32 v58, 16, v101
	v_and_b32_e32 v59, 0xffff0000, v101
	v_and_b32_e32 v99, 0xffff0000, v105
	v_pk_fma_f32 v[58:59], v[60:61], v[98:99], v[58:59]
	s_waitcnt vmcnt(13)
	v_lshlrev_b32_e32 v60, 16, v106
	v_cvt_pk_bf16_f32 v65, v58, v59
	v_lshl_add_u64 v[58:59], s[0:1], 0, v[130:131]
	global_store_dwordx4 v[58:59], v[62:65], off
	v_and_b32_e32 v61, 0xffff0000, v106
	s_waitcnt vmcnt(13)
	v_lshlrev_b32_e32 v62, 16, v110
	v_and_b32_e32 v63, 0xffff0000, v110
	v_pk_fma_f32 v[54:55], v[54:55], v[62:63], v[60:61]
	v_lshlrev_b32_e32 v60, 16, v107
	v_and_b32_e32 v61, 0xffff0000, v107
	v_lshlrev_b32_e32 v62, 16, v111
	v_and_b32_e32 v63, 0xffff0000, v111
	v_pk_fma_f32 v[56:57], v[56:57], v[62:63], v[60:61]
	v_cvt_pk_bf16_f32 v54, v54, v55
	v_cvt_pk_bf16_f32 v55, v56, v57
	v_lshlrev_b32_e32 v56, 16, v108
	v_and_b32_e32 v57, 0xffff0000, v108
	v_lshlrev_b32_e32 v60, 16, v112
	v_and_b32_e32 v61, 0xffff0000, v112
	v_pk_fma_f32 v[46:47], v[46:47], v[60:61], v[56:57]
	v_lshlrev_b32_e32 v60, 16, v113
	v_cvt_pk_bf16_f32 v56, v46, v47
	v_lshlrev_b32_e32 v46, 16, v109
	v_and_b32_e32 v47, 0xffff0000, v109
	v_and_b32_e32 v61, 0xffff0000, v113
	v_pk_fma_f32 v[46:47], v[48:49], v[60:61], v[46:47]
	s_waitcnt vmcnt(11)
	v_lshlrev_b32_e32 v48, 16, v118
	v_cvt_pk_bf16_f32 v57, v46, v47
	v_lshlrev_b32_e32 v46, 16, v114
	v_and_b32_e32 v47, 0xffff0000, v114
	v_and_b32_e32 v49, 0xffff0000, v118
	v_pk_fma_f32 v[46:47], v[50:51], v[48:49], v[46:47]
	v_lshlrev_b32_e32 v48, 16, v115
	v_and_b32_e32 v49, 0xffff0000, v115
	v_lshlrev_b32_e32 v50, 16, v119
	v_and_b32_e32 v51, 0xffff0000, v119
	v_pk_fma_f32 v[48:49], v[52:53], v[50:51], v[48:49]
	v_cvt_pk_bf16_f32 v46, v46, v47
	v_cvt_pk_bf16_f32 v47, v48, v49
	v_lshlrev_b32_e32 v48, 16, v116
	v_and_b32_e32 v49, 0xffff0000, v116
	v_lshlrev_b32_e32 v50, 16, v120
	v_and_b32_e32 v51, 0xffff0000, v120
	v_pk_fma_f32 v[42:43], v[42:43], v[50:51], v[48:49]
	v_lshlrev_b32_e32 v50, 16, v121
	v_cvt_pk_bf16_f32 v48, v42, v43
	v_lshlrev_b32_e32 v42, 16, v117
	v_and_b32_e32 v43, 0xffff0000, v117
	v_and_b32_e32 v51, 0xffff0000, v121
	v_pk_fma_f32 v[42:43], v[44:45], v[50:51], v[42:43]
	s_waitcnt vmcnt(10)
	v_lshlrev_b32_e32 v44, 16, v122
	v_cvt_pk_bf16_f32 v49, v42, v43
	v_add_co_u32_e32 v42, vcc, s86, v58
	v_and_b32_e32 v45, 0xffff0000, v122
	s_nop 0
	v_addc_co_u32_e32 v43, vcc, 0, v59, vcc
	global_store_dwordx4 v[42:43], v[46:49], off
	global_store_dwordx4 v[58:59], v[54:57], off offset:256
	s_waitcnt vmcnt(11)
	v_lshlrev_b32_e32 v46, 16, v126
	v_and_b32_e32 v47, 0xffff0000, v126
	v_pk_fma_f32 v[34:35], v[34:35], v[46:47], v[44:45]
	v_lshlrev_b32_e32 v44, 16, v123
	v_and_b32_e32 v45, 0xffff0000, v123
	v_lshlrev_b32_e32 v46, 16, v127
	v_and_b32_e32 v47, 0xffff0000, v127
	v_pk_fma_f32 v[36:37], v[36:37], v[46:47], v[44:45]
	v_cvt_pk_bf16_f32 v34, v34, v35
	v_cvt_pk_bf16_f32 v35, v36, v37
	v_lshlrev_b32_e32 v36, 16, v124
	v_and_b32_e32 v37, 0xffff0000, v124
	v_lshlrev_b32_e32 v44, 16, v128
	v_and_b32_e32 v45, 0xffff0000, v128
	v_pk_fma_f32 v[22:23], v[22:23], v[44:45], v[36:37]
	v_lshlrev_b32_e32 v44, 16, v129
	v_cvt_pk_bf16_f32 v36, v22, v23
	v_lshlrev_b32_e32 v22, 16, v125
	v_and_b32_e32 v23, 0xffff0000, v125
	v_and_b32_e32 v45, 0xffff0000, v129
	v_pk_fma_f32 v[22:23], v[24:25], v[44:45], v[22:23]
	s_waitcnt vmcnt(9)
; __device__ __forceinline__ unsigned cvt_pk_bf16(float lo, float hi) { return pk2(lo, hi); }
; #define PG8_BAR __builtin_amdgcn_s_barrier()
; template <class Epi, class Sched>
; __device__ __forceinline__ void gemm_phase(PG8_LAS unsigned char* lds, const int K, const Sched& S, const Epi& E, const int wave_s) {
;     ...
;         if (!has_next) break;
; #pragma unroll
;         for (int a = 0; a < 2; ++a)
; #pragma unroll
;             for (int b = 0; b < 2; ++b)
; #pragma unroll
;                 for (int m = 0; m < 4; ++m)
; #pragma unroll
;                     for (int n = 0; n < 2; ++n) acc[a][b][m][n] = (f32x4){0.f, 0.f, 0.f, 0.f};
;         cur = nxt; cA = nA; cB = nB; ++ui;
; #pragma unroll
;         for (int h = 0; h < 2; ++h)
; #pragma unroll
;             for (int i = 0; i < 2; ++i) vA[h][i] = vN[h][i];
;         if (wr == 1) PG8_BAR;
;     __device__ __forceinline__ void operator()(const f32x4 (&acc)[2][2][4][2], const Unit& u, int wr, int wc, int fr, int fq) const {
;     ...
;             for (int m = 0; m < 4; ++m)
; #pragma unroll
;                 for (int bj = 0; bj < 2; ++bj) { const u32x4 x = hv[m][bj], g = gv[m][bj]; const f32x4 a0 = acc[ai][bj][m][0], a1 = acc[ai][bj][m][1];
;                     u32x4 w; w.x = cvt_pk_bf16(bflo(x.x) + a0[0] * bflo(g.x), bfhi(x.x) + a0[1] * bfhi(g.x)); w.y = cvt_pk_bf16(bflo(x.y) + a0[2] * bflo(g.y), bfhi(x.y) + a0[3] * bfhi(g.y));
;                     w.z = cvt_pk_bf16(bflo(x.z) + a1[0] * bflo(g.z), bfhi(x.z) + a1[1] * bfhi(g.z)); w.w = cvt_pk_bf16(bflo(x.w) + a1[2] * bflo(g.w), bfhi(x.w) + a1[3] * bfhi(g.w));
;                     *(u32x4*)(hn + ro0 + (size_t)m * 16 * DM + bj * HALF) = w; }
	v_lshlrev_b32_e32 v24, 16, v94
	v_cvt_pk_bf16_f32 v37, v22, v23
	v_lshlrev_b32_e32 v22, 16, v90
	v_and_b32_e32 v23, 0xffff0000, v90
	v_and_b32_e32 v25, 0xffff0000, v94
	v_pk_fma_f32 v[22:23], v[26:27], v[24:25], v[22:23]
	v_lshlrev_b32_e32 v24, 16, v91
	v_and_b32_e32 v25, 0xffff0000, v91
	v_lshlrev_b32_e32 v26, 16, v95
	v_and_b32_e32 v27, 0xffff0000, v95
	v_pk_fma_f32 v[24:25], v[28:29], v[26:27], v[24:25]
	v_cvt_pk_bf16_f32 v22, v22, v23
	v_cvt_pk_bf16_f32 v23, v24, v25
	v_lshlrev_b32_e32 v24, 16, v92
	v_and_b32_e32 v25, 0xffff0000, v92
	v_lshlrev_b32_e32 v26, 16, v96
	v_and_b32_e32 v27, 0xffff0000, v96
	v_pk_fma_f32 v[18:19], v[18:19], v[26:27], v[24:25]
	v_lshlrev_b32_e32 v26, 16, v97
	v_cvt_pk_bf16_f32 v24, v18, v19
	v_lshlrev_b32_e32 v18, 16, v93
	v_and_b32_e32 v19, 0xffff0000, v93
	v_and_b32_e32 v27, 0xffff0000, v97
	v_pk_fma_f32 v[18:19], v[20:21], v[26:27], v[18:19]
	v_add_co_u32_e32 v26, vcc, s84, v58
	v_cvt_pk_bf16_f32 v25, v18, v19
	s_nop 0
	v_addc_co_u32_e32 v27, vcc, 0, v59, vcc
	s_waitcnt vmcnt(8)
	v_lshlrev_b32_e32 v18, 16, v82
	v_and_b32_e32 v19, 0xffff0000, v82
	s_waitcnt vmcnt(7)
	v_lshlrev_b32_e32 v20, 16, v86
	v_and_b32_e32 v21, 0xffff0000, v86
	global_store_dwordx4 v[26:27], v[22:25], off
	v_pk_fma_f32 v[18:19], v[38:39], v[20:21], v[18:19]
	v_lshlrev_b32_e32 v20, 16, v83
	v_and_b32_e32 v21, 0xffff0000, v83
	v_lshlrev_b32_e32 v22, 16, v87
	v_and_b32_e32 v23, 0xffff0000, v87
	v_pk_fma_f32 v[20:21], v[40:41], v[22:23], v[20:21]
	v_cvt_pk_bf16_f32 v18, v18, v19
	v_cvt_pk_bf16_f32 v19, v20, v21
	v_lshlrev_b32_e32 v20, 16, v84
	v_and_b32_e32 v21, 0xffff0000, v84
	v_lshlrev_b32_e32 v22, 16, v88
	v_and_b32_e32 v23, 0xffff0000, v88
	v_pk_fma_f32 v[20:21], v[30:31], v[22:23], v[20:21]
	v_lshlrev_b32_e32 v22, 16, v85
	v_and_b32_e32 v23, 0xffff0000, v85
	v_lshlrev_b32_e32 v24, 16, v89
	v_and_b32_e32 v25, 0xffff0000, v89
	v_pk_fma_f32 v[22:23], v[32:33], v[24:25], v[22:23]
	v_cvt_pk_bf16_f32 v20, v20, v21
	v_cvt_pk_bf16_f32 v21, v22, v23
	global_store_dwordx4 v[26:27], v[18:21], off offset:256
	global_store_dwordx4 v[42:43], v[34:37], off offset:256
	s_waitcnt vmcnt(9)
	v_lshlrev_b32_e32 v18, 16, v74
	v_and_b32_e32 v19, 0xffff0000, v74
	s_waitcnt vmcnt(8)
	v_lshlrev_b32_e32 v20, 16, v78
	v_and_b32_e32 v21, 0xffff0000, v78
	v_pk_fma_f32 v[6:7], v[6:7], v[20:21], v[18:19]
	v_lshlrev_b32_e32 v18, 16, v75
	v_and_b32_e32 v19, 0xffff0000, v75
	v_lshlrev_b32_e32 v20, 16, v79
	v_and_b32_e32 v21, 0xffff0000, v79
	v_pk_fma_f32 v[8:9], v[8:9], v[20:21], v[18:19]
	v_cvt_pk_bf16_f32 v6, v6, v7
	v_cvt_pk_bf16_f32 v7, v8, v9
	v_lshlrev_b32_e32 v8, 16, v76
	v_and_b32_e32 v9, 0xffff0000, v76
	v_lshlrev_b32_e32 v18, 16, v80
	v_and_b32_e32 v19, 0xffff0000, v80
	v_pk_fma_f32 v[2:3], v[2:3], v[18:19], v[8:9]
	v_lshlrev_b32_e32 v18, 16, v81
	v_cvt_pk_bf16_f32 v8, v2, v3
	v_lshlrev_b32_e32 v2, 16, v77
	v_and_b32_e32 v3, 0xffff0000, v77
	v_and_b32_e32 v19, 0xffff0000, v81
	v_pk_fma_f32 v[2:3], v[4:5], v[18:19], v[2:3]
	v_add_co_u32_e32 v18, vcc, s85, v58
	v_cvt_pk_bf16_f32 v9, v2, v3
	s_nop 0
	v_addc_co_u32_e32 v19, vcc, 0, v59, vcc
	s_waitcnt vmcnt(7)
	v_lshlrev_b32_e32 v2, 16, v66
	v_and_b32_e32 v3, 0xffff0000, v66
	s_waitcnt vmcnt(6)
	v_lshlrev_b32_e32 v4, 16, v70
	v_and_b32_e32 v5, 0xffff0000, v70
	global_store_dwordx4 v[18:19], v[6:9], off
	v_pk_fma_f32 v[2:3], v[14:15], v[4:5], v[2:3]
	v_lshlrev_b32_e32 v4, 16, v67
	v_and_b32_e32 v5, 0xffff0000, v67
	v_lshlrev_b32_e32 v6, 16, v71
	v_and_b32_e32 v7, 0xffff0000, v71
	v_pk_fma_f32 v[4:5], v[16:17], v[6:7], v[4:5]
	v_cvt_pk_bf16_f32 v2, v2, v3
	v_cvt_pk_bf16_f32 v3, v4, v5
	v_lshlrev_b32_e32 v4, 16, v68
	v_and_b32_e32 v5, 0xffff0000, v68
	v_lshlrev_b32_e32 v6, 16, v72
	v_and_b32_e32 v7, 0xffff0000, v72
	v_pk_fma_f32 v[4:5], v[10:11], v[6:7], v[4:5]
	v_lshlrev_b32_e32 v6, 16, v69
	v_and_b32_e32 v7, 0xffff0000, v69
	v_lshlrev_b32_e32 v8, 16, v73
	v_and_b32_e32 v9, 0xffff0000, v73
	v_pk_fma_f32 v[6:7], v[12:13], v[8:9], v[6:7]
	v_cvt_pk_bf16_f32 v4, v4, v5
	v_cvt_pk_bf16_f32 v5, v6, v7
	global_store_dwordx4 v[18:19], v[2:5], off offset:256
	s_and_b64 vcc, exec, s[4:5]
	s_cbranch_vccnz .LBB0_1197
	s_andn2_b64 vcc, exec, s[2:3]
	s_cbranch_vccnz .LBB0_1196
	s_barrier
	s_branch .LBB0_1196
